# placement: pad nops restore the baseline byte phase (offset within a 64-byte fetch line) of all hot loop heads
# speedup vs baseline: 1.0042x; 1.0042x over previous
.LBB0_488:
	s_ashr_i32 s21, s20, 31
	s_lshl_b64 s[24:25], s[20:21], 19
	s_add_u32 s24, s43, s24
	s_addc_u32 s25, s44, s25
	s_and_b64 s[30:31], s[30:31], exec
	s_cselect_b32 s11, s25, s29
	s_cselect_b32 s19, s24, s28
	s_add_u32 s26, s26, 0x40080
	s_addc_u32 s27, s27, 0
	s_add_u32 s21, s28, 0x100
	v_mov_b32_e32 v2, 0
	s_addc_u32 s49, s29, 0
	s_mov_b32 s67, -2
	v_mov_b32_e32 v3, v2
	v_mov_b32_e32 v4, v2
	v_mov_b32_e32 v5, v2
	v_mov_b32_e32 v6, v2
	v_mov_b32_e32 v7, v2
	v_mov_b32_e32 v8, v2
	v_mov_b32_e32 v9, v2
	v_mov_b32_e32 v18, v2
	v_mov_b32_e32 v19, v2
	v_mov_b32_e32 v20, v2
	v_mov_b32_e32 v21, v2
	v_mov_b32_e32 v22, v2
	v_mov_b32_e32 v23, v2
	v_mov_b32_e32 v24, v2
	v_mov_b32_e32 v25, v2
	v_mov_b32_e32 v34, v2
	v_mov_b32_e32 v35, v2
	v_mov_b32_e32 v36, v2
	v_mov_b32_e32 v37, v2
	v_mov_b32_e32 v38, v2
	v_mov_b32_e32 v39, v2
	v_mov_b32_e32 v40, v2
	v_mov_b32_e32 v41, v2
	v_mov_b32_e32 v50, v2
	v_mov_b32_e32 v51, v2
	v_mov_b32_e32 v52, v2
	v_mov_b32_e32 v53, v2
	v_mov_b32_e32 v54, v2
	v_mov_b32_e32 v55, v2
	v_mov_b32_e32 v56, v2
	v_mov_b32_e32 v57, v2
	v_mov_b32_e32 v10, v2
	v_mov_b32_e32 v11, v2
	v_mov_b32_e32 v12, v2
	v_mov_b32_e32 v13, v2
	v_mov_b32_e32 v14, v2
	v_mov_b32_e32 v15, v2
	v_mov_b32_e32 v16, v2
	v_mov_b32_e32 v17, v2
	v_mov_b32_e32 v26, v2
	v_mov_b32_e32 v27, v2
	v_mov_b32_e32 v28, v2
	v_mov_b32_e32 v29, v2
	v_mov_b32_e32 v30, v2
	v_mov_b32_e32 v31, v2
	v_mov_b32_e32 v32, v2
	v_mov_b32_e32 v33, v2
	v_mov_b32_e32 v42, v2
	v_mov_b32_e32 v43, v2
	v_mov_b32_e32 v44, v2
	v_mov_b32_e32 v45, v2
	v_mov_b32_e32 v46, v2
	v_mov_b32_e32 v47, v2
	v_mov_b32_e32 v48, v2
	v_mov_b32_e32 v49, v2
	v_mov_b32_e32 v58, v2
	v_mov_b32_e32 v59, v2
	v_mov_b32_e32 v60, v2
	v_mov_b32_e32 v61, v2
	v_mov_b32_e32 v62, v2
	v_mov_b32_e32 v63, v2
	v_mov_b32_e32 v64, v2
	v_mov_b32_e32 v65, v2
	v_mov_b32_e32 v66, v2
	v_mov_b32_e32 v67, v2
	v_mov_b32_e32 v68, v2
	v_mov_b32_e32 v69, v2
	v_mov_b32_e32 v70, v2
	v_mov_b32_e32 v71, v2
	v_mov_b32_e32 v72, v2
	v_mov_b32_e32 v73, v2
	v_mov_b32_e32 v82, v2
	v_mov_b32_e32 v83, v2
	v_mov_b32_e32 v84, v2
	v_mov_b32_e32 v85, v2
	v_mov_b32_e32 v86, v2
	v_mov_b32_e32 v87, v2
	v_mov_b32_e32 v88, v2
	v_mov_b32_e32 v89, v2
	v_mov_b32_e32 v106, v2
	v_mov_b32_e32 v107, v2
	v_mov_b32_e32 v108, v2
	v_mov_b32_e32 v109, v2
	v_mov_b32_e32 v110, v2
	v_mov_b32_e32 v111, v2
	v_mov_b32_e32 v112, v2
	v_mov_b32_e32 v113, v2
	v_mov_b32_e32 v130, v2
	v_mov_b32_e32 v131, v2
	v_mov_b32_e32 v132, v2
	v_mov_b32_e32 v133, v2
	v_mov_b32_e32 v134, v2
	v_mov_b32_e32 v135, v2
	v_mov_b32_e32 v136, v2
	v_mov_b32_e32 v137, v2
	v_mov_b32_e32 v74, v2
	v_mov_b32_e32 v75, v2
	v_mov_b32_e32 v76, v2
	v_mov_b32_e32 v77, v2
	v_mov_b32_e32 v78, v2
	v_mov_b32_e32 v79, v2
	v_mov_b32_e32 v80, v2
	v_mov_b32_e32 v81, v2
	v_mov_b32_e32 v90, v2
	v_mov_b32_e32 v91, v2
	v_mov_b32_e32 v92, v2
	v_mov_b32_e32 v93, v2
	v_mov_b32_e32 v94, v2
	v_mov_b32_e32 v95, v2
	v_mov_b32_e32 v96, v2
	v_mov_b32_e32 v97, v2
	v_mov_b32_e32 v122, v2
	v_mov_b32_e32 v123, v2
	v_mov_b32_e32 v124, v2
	v_mov_b32_e32 v125, v2
	v_mov_b32_e32 v126, v2
	v_mov_b32_e32 v127, v2
	v_mov_b32_e32 v128, v2
	v_mov_b32_e32 v129, v2
	v_mov_b32_e32 v138, v2
	v_mov_b32_e32 v139, v2
	v_mov_b32_e32 v140, v2
	v_mov_b32_e32 v141, v2
	v_mov_b32_e32 v142, v2
	v_mov_b32_e32 v143, v2
	v_mov_b32_e32 v144, v2
	v_mov_b32_e32 v145, v2
	s_nop 0
	s_nop 0
	s_nop 0
	s_nop 0
	s_nop 0
	s_nop 0
	s_nop 0
	s_nop 0
	s_nop 0
	s_nop 0

.LBB0_935:
	s_mov_b32 s10, 35
	s_waitcnt lgkmcnt(0)
	s_barrier
	s_ashr_i32 s11, s10, 31
	s_ashr_i32 s12, s9, 6
	s_lshl_b64 s[10:11], s[10:11], 3
	s_add_u32 s10, s0, s10
	s_addc_u32 s11, s1, s11
	s_load_dwordx2 s[10:11], s[10:11], 0x0
	v_bfe_u32 v9, v176, 1, 3
	v_lshl_add_u32 v2, v9, 8, s8
	v_and_b32_e32 v177, 1, v176
	v_ashrrev_i32_e32 v3, 31, v2
	v_bfe_u32 v8, v0, 4, 2
	v_lshlrev_b64 v[4:5], 13, v[2:3]
	v_lshlrev_b32_e32 v6, 6, v177
	v_lshlrev_b32_e32 v172, 3, v8
	s_waitcnt lgkmcnt(0)
	v_lshl_add_u64 v[4:5], s[10:11], 0, v[4:5]
	v_mov_b32_e32 v173, v1
	v_lshl_or_b32 v6, s12, 9, v6
	v_lshl_add_u64 v[4:5], v[4:5], 0, v[172:173]
	v_ashrrev_i32_e32 v7, 31, v6
	v_lshl_add_u64 v[4:5], v[6:7], 1, v[4:5]
	s_mov_b64 s[8:9], 0x35400000
	v_lshl_add_u64 v[6:7], v[4:5], 0, s[8:9]
	s_mov_b32 s8, 0x35400000
	v_add_co_u32_e32 v4, vcc, s8, v4
	s_movk_i32 s8, 0xffc
	s_nop 0
	v_addc_co_u32_e32 v5, vcc, 0, v5, vcc
	global_load_dwordx2 v[168:169], v[6:7], off offset:32
	global_load_dwordx2 v[166:167], v[6:7], off offset:64
	global_load_dwordx2 v[164:165], v[6:7], off offset:96
	global_load_dwordx2 v[162:163], v[6:7], off offset:256
	global_load_dwordx2 v[160:161], v[6:7], off offset:288
	global_load_dwordx2 v[158:159], v[6:7], off offset:320
	global_load_dwordx2 v[156:157], v[6:7], off offset:352
	global_load_dwordx2 v[154:155], v[6:7], off offset:512
	global_load_dwordx2 v[152:153], v[6:7], off offset:544
	global_load_dwordx2 v[150:151], v[6:7], off offset:576
	global_load_dwordx2 v[148:149], v[6:7], off offset:608
	global_load_dwordx2 v[146:147], v[6:7], off offset:768
	global_load_dwordx2 v[170:171], v[4:5], off
	global_load_dwordx2 v[144:145], v[6:7], off offset:800
	global_load_dwordx2 v[142:143], v[6:7], off offset:832
	global_load_dwordx2 v[140:141], v[6:7], off offset:864
	v_and_b32_e32 v4, 15, v176
	v_mov_b32_e32 v5, 0xfff
	v_lshrrev_b32_e32 v173, 4, v0
	v_bitop3_b32 v0, v4, 3, v5 bitop3:0x48
	v_bitop3_b32 v4, v4, s8, v5 bitop3:0x48
	v_add_u32_e32 v4, v172, v4
	v_mul_u32_u24_e32 v178, 0x2020, v9
	v_lshlrev_b32_e32 v179, 4, v8
	v_lshlrev_b64 v[174:175], 12, v[2:3]
	v_mul_u32_u24_e32 v0, 0x4040, v0
	s_lshl_b32 s18, s12, 3
	s_sub_i32 s20, s18, 63
	v_lshl_add_u32 v180, v4, 1, v0
	s_lshl_b32 s8, s20, 7
	v_subrev_u32_e32 v0, s8, v180
	v_add_u32_e32 v0, 0, v0
	v_subrev_u32_e32 v2, 32, v0
	ds_read_b64 v[124:125], v0 offset:64
	ds_read_b64 v[126:127], v0 offset:72
	ds_read_b64 v[128:129], v0 offset:32
	ds_read_b64 v[130:131], v0 offset:40
	ds_read_b64 v[132:133], v0
	ds_read_b64 v[134:135], v0 offset:8
	ds_read_b64 v[136:137], v2
	v_subrev_u32_e32 v2, 24, v0
	ds_read_b64 v[138:139], v2
	v_subrev_u32_e32 v2, 64, v0
	ds_read_b64 v[68:69], v2
	v_subrev_u32_e32 v2, 56, v0
	ds_read_b64 v[70:71], v2
	v_add_u32_e32 v2, 0xffffffa0, v0
	v_add_u32_e32 v0, 0xffffffa8, v0
	ds_read_b64 v[72:73], v2
	ds_read_b64 v[74:75], v0
	v_lshlrev_b32_e32 v0, 7, v177
	s_movk_i32 s8, 0x2020
	v_mad_u32_u24 v0, v9, s8, v0
	s_mov_b32 s8, 0x12080
	v_mov_b32_e32 v2, v1
	v_mov_b32_e32 v3, v1
	v_add3_u32 v184, v0, v179, s8
	v_mov_b32_e32 v0, v1
	v_mov_b64_e32 v[6:7], v[2:3]
	v_mov_b64_e32 v[22:23], v[2:3]
	v_mov_b64_e32 v[38:39], v[2:3]
	v_mov_b64_e32 v[54:55], v[2:3]
	v_mov_b64_e32 v[10:11], v[2:3]
	v_mov_b64_e32 v[26:27], v[2:3]
	v_mov_b64_e32 v[42:43], v[2:3]
	v_mov_b64_e32 v[58:59], v[2:3]
	v_mov_b64_e32 v[14:15], v[2:3]
	v_mov_b64_e32 v[30:31], v[2:3]
	v_mov_b64_e32 v[46:47], v[2:3]
	v_mov_b64_e32 v[62:63], v[2:3]
	v_mov_b64_e32 v[18:19], v[2:3]
	v_mov_b64_e32 v[34:35], v[2:3]
	v_mov_b64_e32 v[50:51], v[2:3]
	v_mov_b64_e32 v[66:67], v[2:3]
	s_or_b32 s19, s18, 7
	v_subrev_u32_e32 v183, 32, v180
	v_subrev_u32_e32 v182, 64, v180
	v_add_u32_e32 v181, 0xffffffa0, v180
	s_movk_i32 s21, 0x46
	v_mov_b64_e32 v[4:5], v[0:1]
	v_mov_b64_e32 v[20:21], v[0:1]
	v_mov_b64_e32 v[36:37], v[0:1]
	v_mov_b64_e32 v[52:53], v[0:1]
	v_mov_b64_e32 v[8:9], v[0:1]
	v_mov_b64_e32 v[24:25], v[0:1]
	v_mov_b64_e32 v[40:41], v[0:1]
	v_mov_b64_e32 v[56:57], v[0:1]
	v_mov_b64_e32 v[12:13], v[0:1]
	v_mov_b64_e32 v[28:29], v[0:1]
	v_mov_b64_e32 v[44:45], v[0:1]
	v_mov_b64_e32 v[60:61], v[0:1]
	v_mov_b64_e32 v[16:17], v[0:1]
	v_mov_b64_e32 v[32:33], v[0:1]
	v_mov_b64_e32 v[48:49], v[0:1]
	v_mov_b64_e32 v[64:65], v[0:1]
	s_nop 0
	s_nop 0
	s_nop 0
	s_nop 0
	s_nop 0
	s_nop 0
	s_nop 0
	s_nop 0
	s_nop 0
	s_nop 0
	s_nop 0
	s_nop 0
	s_nop 0

.LBB0_1067:
	s_and_b32 s10, s13, 0x3fffffc0
	v_add_f32_e32 v235, v1, v37
	s_lshl_b32 s10, s10, 2
	v_xor_b32_e32 v48, 0x80000000, v235
	v_mov_b32_e32 v49, v48
	v_mov_b32_e32 v50, v48
	v_mov_b32_e32 v51, v48
	v_mov_b32_e32 v52, v48
	v_mov_b32_e32 v53, v48
	v_mov_b32_e32 v54, v48
	v_mov_b32_e32 v55, v48
	v_mov_b32_e32 v56, v48
	v_mov_b32_e32 v57, v48
	v_mov_b32_e32 v58, v48
	v_mov_b32_e32 v59, v48
	v_mov_b32_e32 v60, v48
	v_mov_b32_e32 v61, v48
	v_mov_b32_e32 v62, v48
	v_mov_b32_e32 v63, v48
	s_add_i32 s13, s10, 0
	v_sub_f32_e32 v2, v2, v37
	v_sub_f32_e32 v3, v3, v37
	s_waitcnt vmcnt(0) lgkmcnt(0)
	s_barrier
	s_mov_b64 s[10:11], 0x6000
	v_exp_f32_e32 v64, v2
	v_exp_f32_e32 v65, v3
	v_lshl_add_u64 v[2:3], v[34:35], 0, s[10:11]
	s_mov_b32 s10, m0
	s_mov_b32 m0, s45
	s_nop 0
	global_load_lds_dwordx4 v[2:3], off
	s_mov_b32 m0, s10
	s_cmp_lg_u32 0, -1
	s_cselect_b32 s10, 0, 0
	s_add_i32 s10, s10, s12
	v_lshl_add_u64 v[2:3], v[208:209], 0, s[70:71]
	s_add_i32 s10, s10, 0x8000
	s_mov_b32 s11, m0
	s_mov_b32 m0, s10
	s_nop 0
	global_load_lds_dwordx4 v[2:3], off
	s_mov_b32 m0, s11
	ds_read_b128 v[188:191], v240 offset:8192
	ds_read_b128 v[184:187], v240 offset:8704
	ds_read_b128 v[180:183], v240 offset:10240
	ds_read_b128 v[176:179], v240 offset:10752
	ds_read_b128 v[172:175], v240 offset:12288
	ds_read_b128 v[168:171], v240 offset:12800
	ds_read_b128 v[164:167], v240 offset:14336
	ds_read_b128 v[160:163], v240 offset:14848
	v_lshlrev_b32_e32 v0, 1, v36
	v_and_b32_e32 v236, 32, v0
	v_lshlrev_b32_e32 v241, 2, v232
	v_lshrrev_b32_e32 v0, 2, v36
	v_and_or_b32 v0, v0, 3, v241
	v_lshlrev_b32_e32 v237, 6, v0
	v_sub_f32_e32 v0, v18, v37
	v_sub_f32_e32 v18, v19, v37
	v_sub_f32_e32 v19, v20, v37
	v_sub_f32_e32 v4, v4, v37
	v_sub_f32_e32 v20, v21, v37
	v_sub_f32_e32 v5, v5, v37
	v_sub_f32_e32 v21, v22, v37
	v_sub_f32_e32 v6, v6, v37
	v_sub_f32_e32 v22, v23, v37
	v_sub_f32_e32 v7, v7, v37
	v_sub_f32_e32 v23, v24, v37
	v_sub_f32_e32 v8, v8, v37
	v_sub_f32_e32 v24, v25, v37
	v_sub_f32_e32 v9, v9, v37
	v_sub_f32_e32 v25, v26, v37
	v_sub_f32_e32 v10, v10, v37
	v_sub_f32_e32 v26, v27, v37
	v_sub_f32_e32 v11, v11, v37
	v_sub_f32_e32 v27, v28, v37
	v_sub_f32_e32 v12, v12, v37
	v_sub_f32_e32 v28, v29, v37
	v_sub_f32_e32 v13, v13, v37
	v_sub_f32_e32 v29, v30, v37
	v_sub_f32_e32 v14, v14, v37
	v_sub_f32_e32 v30, v31, v37
	v_sub_f32_e32 v15, v15, v37
	v_sub_f32_e32 v31, v32, v37
	v_sub_f32_e32 v16, v16, v37
	v_sub_f32_e32 v32, v33, v37
	v_sub_f32_e32 v17, v17, v37
	s_nop 0
	v_exp_f32_e32 v80, v0
	v_exp_f32_e32 v81, v18
	v_exp_f32_e32 v82, v19
	v_exp_f32_e32 v83, v20
	v_exp_f32_e32 v84, v21
	v_exp_f32_e32 v85, v22
	v_exp_f32_e32 v86, v23
	v_exp_f32_e32 v87, v24
	v_exp_f32_e32 v88, v25
	v_exp_f32_e32 v89, v26
	v_exp_f32_e32 v90, v27
	v_exp_f32_e32 v91, v28
	v_exp_f32_e32 v92, v29
	v_exp_f32_e32 v93, v30
	v_exp_f32_e32 v94, v31
	v_exp_f32_e32 v95, v32
	v_exp_f32_e32 v66, v4
	v_exp_f32_e32 v67, v5
	v_exp_f32_e32 v68, v6
	v_exp_f32_e32 v69, v7
	v_exp_f32_e32 v70, v8
	v_exp_f32_e32 v71, v9
	v_exp_f32_e32 v72, v10
	v_exp_f32_e32 v73, v11
	v_exp_f32_e32 v74, v12
	v_exp_f32_e32 v75, v13
	v_exp_f32_e32 v76, v14
	v_exp_f32_e32 v77, v15
	v_exp_f32_e32 v78, v16
	v_exp_f32_e32 v79, v17
	s_cmp_lt_i32 s63, 7
	s_waitcnt vmcnt(2) lgkmcnt(0)
	s_barrier
	s_cselect_b64 s[10:11], -1, 0
	v_add_u32_e32 v36, 0, v236
	s_or_b64 s[10:11], s[30:31], s[10:11]
	s_mov_b32 s34, 1
	v_add3_u32 v242, v36, v234, v237
	s_mov_b32 s40, 0
	s_and_b64 vcc, exec, s[10:11]
	v_cmp_gt_u32_e64 s[10:11], 32, v211
	v_lshl_add_u32 v239, v231, 2, s13
	v_lshl_add_u32 v238, v241, 2, s13
	s_cbranch_vccnz .LBB0_1086
	v_mov_b32_e32 v14, v1
	v_mov_b32_e32 v15, v1
	v_mov_b32_e32 v0, v1
	v_mov_b32_e32 v2, v1
	v_mov_b32_e32 v3, v1
	v_mov_b32_e32 v4, v1
	v_mov_b32_e32 v5, v1
	v_mov_b32_e32 v6, v1
	v_mov_b32_e32 v7, v1
	v_mov_b32_e32 v8, v1
	v_mov_b32_e32 v9, v1
	v_mov_b32_e32 v10, v1
	v_mov_b32_e32 v11, v1
	v_mov_b32_e32 v12, v1
	v_mov_b32_e32 v13, v1
	v_mov_b64_e32 v[46:47], v[14:15]
	v_mov_b64_e32 v[30:31], v[14:15]
	s_add_i32 s41, s63, -7
	s_mov_b32 s12, 0
	s_movk_i32 s40, 0x4000
	s_movk_i32 s49, 0x2000
	v_mov_b32_e32 v243, 0
	s_mov_b32 s77, -1
	s_movk_i32 s84, 0xc0
	v_mov_b64_e32 v[44:45], v[12:13]
	v_mov_b64_e32 v[42:43], v[10:11]
	v_mov_b64_e32 v[40:41], v[8:9]
	v_mov_b64_e32 v[38:39], v[6:7]
	v_mov_b64_e32 v[36:37], v[4:5]
	v_mov_b64_e32 v[34:35], v[2:3]
	v_mov_b64_e32 v[32:33], v[0:1]
	v_mov_b64_e32 v[28:29], v[12:13]
	v_mov_b64_e32 v[26:27], v[10:11]
	v_mov_b64_e32 v[24:25], v[8:9]
	v_mov_b64_e32 v[22:23], v[6:7]
	v_mov_b64_e32 v[20:21], v[4:5]
	v_mov_b64_e32 v[18:19], v[2:3]
	v_mov_b64_e32 v[16:17], v[0:1]
	s_nop 0
	s_nop 0
	s_nop 0
	s_nop 0
	s_nop 0
	s_nop 0
	s_nop 0
	s_nop 0
	s_nop 0
	s_nop 0
	s_nop 0
	s_nop 0
	s_nop 0
	s_nop 0

.LBB0_1388:
	s_ashr_i32 s21, s20, 31
	s_lshl_b64 s[24:25], s[20:21], 19
	s_add_u32 s24, s45, s24
	s_addc_u32 s25, s46, s25
	s_and_b64 s[34:35], s[34:35], exec
	s_cselect_b32 s19, s25, s31
	s_cselect_b32 s21, s24, s30
	s_add_u32 s28, s28, 0x40080
	s_addc_u32 s29, s29, 0
	s_add_u32 s49, s30, 0x100
	v_mov_b32_e32 v2, 0
	s_addc_u32 s76, s31, 0
	s_mov_b32 s77, -2
	v_mov_b32_e32 v3, v2
	v_mov_b32_e32 v4, v2
	v_mov_b32_e32 v5, v2
	v_mov_b32_e32 v6, v2
	v_mov_b32_e32 v7, v2
	v_mov_b32_e32 v8, v2
	v_mov_b32_e32 v9, v2
	v_mov_b32_e32 v18, v2
	v_mov_b32_e32 v19, v2
	v_mov_b32_e32 v20, v2
	v_mov_b32_e32 v21, v2
	v_mov_b32_e32 v22, v2
	v_mov_b32_e32 v23, v2
	v_mov_b32_e32 v24, v2
	v_mov_b32_e32 v25, v2
	v_mov_b32_e32 v34, v2
	v_mov_b32_e32 v35, v2
	v_mov_b32_e32 v36, v2
	v_mov_b32_e32 v37, v2
	v_mov_b32_e32 v38, v2
	v_mov_b32_e32 v39, v2
	v_mov_b32_e32 v40, v2
	v_mov_b32_e32 v41, v2
	v_mov_b32_e32 v50, v2
	v_mov_b32_e32 v51, v2
	v_mov_b32_e32 v52, v2
	v_mov_b32_e32 v53, v2
	v_mov_b32_e32 v54, v2
	v_mov_b32_e32 v55, v2
	v_mov_b32_e32 v56, v2
	v_mov_b32_e32 v57, v2
	v_mov_b32_e32 v10, v2
	v_mov_b32_e32 v11, v2
	v_mov_b32_e32 v12, v2
	v_mov_b32_e32 v13, v2
	v_mov_b32_e32 v14, v2
	v_mov_b32_e32 v15, v2
	v_mov_b32_e32 v16, v2
	v_mov_b32_e32 v17, v2
	v_mov_b32_e32 v26, v2
	v_mov_b32_e32 v27, v2
	v_mov_b32_e32 v28, v2
	v_mov_b32_e32 v29, v2
	v_mov_b32_e32 v30, v2
	v_mov_b32_e32 v31, v2
	v_mov_b32_e32 v32, v2
	v_mov_b32_e32 v33, v2
	v_mov_b32_e32 v42, v2
	v_mov_b32_e32 v43, v2
	v_mov_b32_e32 v44, v2
	v_mov_b32_e32 v45, v2
	v_mov_b32_e32 v46, v2
	v_mov_b32_e32 v47, v2
	v_mov_b32_e32 v48, v2
	v_mov_b32_e32 v49, v2
	v_mov_b32_e32 v58, v2
	v_mov_b32_e32 v59, v2
	v_mov_b32_e32 v60, v2
	v_mov_b32_e32 v61, v2
	v_mov_b32_e32 v62, v2
	v_mov_b32_e32 v63, v2
	v_mov_b32_e32 v64, v2
	v_mov_b32_e32 v65, v2
	v_mov_b32_e32 v66, v2
	v_mov_b32_e32 v67, v2
	v_mov_b32_e32 v68, v2
	v_mov_b32_e32 v69, v2
	v_mov_b32_e32 v70, v2
	v_mov_b32_e32 v71, v2
	v_mov_b32_e32 v72, v2
	v_mov_b32_e32 v73, v2
	v_mov_b32_e32 v82, v2
	v_mov_b32_e32 v83, v2
	v_mov_b32_e32 v84, v2
	v_mov_b32_e32 v85, v2
	v_mov_b32_e32 v86, v2
	v_mov_b32_e32 v87, v2
	v_mov_b32_e32 v88, v2
	v_mov_b32_e32 v89, v2
	v_mov_b32_e32 v98, v2
	v_mov_b32_e32 v99, v2
	v_mov_b32_e32 v100, v2
	v_mov_b32_e32 v101, v2
	v_mov_b32_e32 v102, v2
	v_mov_b32_e32 v103, v2
	v_mov_b32_e32 v104, v2
	v_mov_b32_e32 v105, v2
	v_mov_b32_e32 v114, v2
	v_mov_b32_e32 v115, v2
	v_mov_b32_e32 v116, v2
	v_mov_b32_e32 v117, v2
	v_mov_b32_e32 v118, v2
	v_mov_b32_e32 v119, v2
	v_mov_b32_e32 v120, v2
	v_mov_b32_e32 v121, v2
	v_mov_b32_e32 v74, v2
	v_mov_b32_e32 v75, v2
	v_mov_b32_e32 v76, v2
	v_mov_b32_e32 v77, v2
	v_mov_b32_e32 v78, v2
	v_mov_b32_e32 v79, v2
	v_mov_b32_e32 v80, v2
	v_mov_b32_e32 v81, v2
	v_mov_b32_e32 v90, v2
	v_mov_b32_e32 v91, v2
	v_mov_b32_e32 v92, v2
	v_mov_b32_e32 v93, v2
	v_mov_b32_e32 v94, v2
	v_mov_b32_e32 v95, v2
	v_mov_b32_e32 v96, v2
	v_mov_b32_e32 v97, v2
	v_mov_b32_e32 v106, v2
	v_mov_b32_e32 v107, v2
	v_mov_b32_e32 v108, v2
	v_mov_b32_e32 v109, v2
	v_mov_b32_e32 v110, v2
	v_mov_b32_e32 v111, v2
	v_mov_b32_e32 v112, v2
	v_mov_b32_e32 v113, v2
	v_mov_b32_e32 v122, v2
	v_mov_b32_e32 v123, v2
	v_mov_b32_e32 v124, v2
	v_mov_b32_e32 v125, v2
	v_mov_b32_e32 v126, v2
	v_mov_b32_e32 v127, v2
	v_mov_b32_e32 v128, v2
	v_mov_b32_e32 v129, v2
	s_nop 0
	s_nop 0
	s_nop 0
	s_nop 0
	s_nop 0
	s_nop 0
	s_nop 0
	s_nop 0
	s_nop 0
	s_nop 0
	s_nop 0
	s_nop 0
	s_nop 0
	s_nop 0

.LBB0_1787:
	s_nop 0
	s_lshl_b32 s20, s63, 10
	s_add_i32 s20, s20, 0
	s_add_i32 s20, s20, 0x20800
	s_add_u32 s68, s18, 0x100
	v_lshl_add_u32 v209, v170, 2, s20
	v_lshl_add_u32 v210, v171, 2, s20
	s_addc_u32 s69, s19, 0
	s_mov_b32 s70, -2
	s_mov_b64 s[18:19], s[10:11]
	ds_read_b32 v0, v209 offset:512
	ds_read_b32 v166, v210 offset:512
	ds_read_b128 v[22:25], v186
	ds_read_b128 v[18:21], v175
	ds_read_b128 v[26:29], v176
	ds_read_b128 v[30:33], v187
	ds_read_b128 v[6:9], v188
	ds_read_b128 v[2:5], v177
	ds_read_b128 v[10:13], v178
	ds_read_b128 v[14:17], v189
	s_add_u32 s22, s18, 0x80
	s_addc_u32 s23, s19, 0
	s_cmp_eq_u32 s70, 4
	s_cselect_b64 s[24:25], -1, 0
	s_and_b64 s[20:21], s[24:25], exec
	s_cselect_b32 s21, s5, s23
	s_cselect_b32 s20, s4, s22
	s_cselect_b32 s22, s14, s68
	s_cselect_b32 s23, s15, s69
	s_and_b64 s[24:25], s[16:17], s[24:25]
	v_add_u32_e32 v211, 0, v174
	s_waitcnt lgkmcnt(0)
	v_lshl_or_b32 v0, v0, 10, v173
	s_add_i32 m0, s31, 0xc000
	ds_read_b128 v[230:233], v211
	ds_read_b128 v[238:241], v211 offset:2048
	ds_read_b128 v[234:237], v190
	ds_read_b128 v[242:245], v190 offset:2048
	ds_read_b128 v[246:249], v211 offset:4096
	ds_read_b128 v[222:225], v211 offset:6144
	ds_read_b128 v[250:253], v190 offset:4096
	ds_read_b128 v[226:229], v190 offset:6144
	global_load_lds_dwordx4 v0, s[18:19]
	v_lshl_or_b32 v0, v166, 10, v173
	s_add_i32 m0, s31, 0xe000
	s_nop 0
	global_load_lds_dwordx4 v0, s[18:19]
	s_waitcnt vmcnt(8)
	s_waitcnt lgkmcnt(0)
	s_barrier
	s_setprio 1
	s_waitcnt lgkmcnt(0)
	v_mfma_scale_f32_16x16x128_f8f6f4 v[158:161], v[18:25], v[230:237], 0, v172, v172 op_sel_hi:[0,0,0]
	v_mfma_scale_f32_16x16x128_f8f6f4 v[150:153], v[26:33], v[230:237], 0, v172, v172 op_sel_hi:[0,0,0]
	v_mfma_scale_f32_16x16x128_f8f6f4 v[142:145], v[18:25], v[238:245], 0, v172, v172 op_sel_hi:[0,0,0]
	v_mfma_scale_f32_16x16x128_f8f6f4 v[134:137], v[26:33], v[238:245], 0, v172, v172 op_sel_hi:[0,0,0]
	v_mfma_scale_f32_16x16x128_f8f6f4 v[126:129], v[18:25], v[246:253], 0, v172, v172 op_sel_hi:[0,0,0]
	v_mfma_scale_f32_16x16x128_f8f6f4 v[118:121], v[26:33], v[246:253], 0, v172, v172 op_sel_hi:[0,0,0]
	v_mfma_scale_f32_16x16x128_f8f6f4 v[110:113], v[18:25], v[222:229], 0, v172, v172 op_sel_hi:[0,0,0]
	v_mfma_scale_f32_16x16x128_f8f6f4 v[102:105], v[26:33], v[222:229], 0, v172, v172 op_sel_hi:[0,0,0]
	s_setprio 0
	s_setprio 1
	s_and_b64 s[24:25], s[24:25], exec
	v_mfma_scale_f32_16x16x128_f8f6f4 v[154:157], v[2:9], v[230:237], 0, v172, v172 op_sel_hi:[0,0,0]
	v_mfma_scale_f32_16x16x128_f8f6f4 v[146:149], v[10:17], v[230:237], 0, v172, v172 op_sel_hi:[0,0,0]
	v_mfma_scale_f32_16x16x128_f8f6f4 v[138:141], v[2:9], v[238:245], 0, v172, v172 op_sel_hi:[0,0,0]
	v_mfma_scale_f32_16x16x128_f8f6f4 v[130:133], v[10:17], v[238:245], 0, v172, v172 op_sel_hi:[0,0,0]
	v_mfma_scale_f32_16x16x128_f8f6f4 v[122:125], v[2:9], v[246:253], 0, v172, v172 op_sel_hi:[0,0,0]
	v_mfma_scale_f32_16x16x128_f8f6f4 v[114:117], v[10:17], v[246:253], 0, v172, v172 op_sel_hi:[0,0,0]
	v_mfma_scale_f32_16x16x128_f8f6f4 v[106:109], v[2:9], v[222:229], 0, v172, v172 op_sel_hi:[0,0,0]
	v_mfma_scale_f32_16x16x128_f8f6f4 v[98:101], v[10:17], v[222:229], 0, v172, v172 op_sel_hi:[0,0,0]
	s_cselect_b32 s24, s53, s63
	s_setprio 0
	s_barrier
	s_lshl_b32 s24, s24, 10
	s_add_i32 s24, s24, 0
	s_add_i32 s24, s24, 0x20800
	v_lshl_add_u32 v0, v170, 2, s24
	v_lshl_add_u32 v214, v171, 2, s24
	ds_read_b32 v166, v0
	ds_read_b32 v167, v214
	ds_read_b128 v[226:229], v191
	s_mov_b32 m0, s34
	s_add_u32 s24, s22, 0x20000
	s_waitcnt lgkmcnt(0)
	v_lshl_or_b32 v215, v166, 10, v173
	v_lshl_or_b32 v216, v167, 10, v173
	v_lshl_add_u64 v[166:167], s[22:23], 0, v[164:165]
	ds_read_b128 v[222:225], v211 offset:16384
	ds_read_b128 v[230:233], v211 offset:18432
	ds_read_b128 v[234:237], v192
	ds_read_b128 v[242:245], v193
	ds_read_b128 v[238:241], v211 offset:20480
	ds_read_b128 v[246:249], v211 offset:22528
	ds_read_b128 v[250:253], v194
	global_load_lds_dwordx4 v[166:167], off
	v_lshl_add_u64 v[168:169], s[22:23], 0, v[162:163]
	s_mov_b32 m0, s35
	s_addc_u32 s25, s23, 0
	global_load_lds_dwordx4 v[168:169], off
	v_lshl_add_u64 v[212:213], s[24:25], 0, v[164:165]
	s_mov_b32 m0, s36
	s_nop 0
	global_load_lds_dwordx4 v[212:213], off
	v_lshl_add_u64 v[212:213], s[24:25], 0, v[162:163]
	s_mov_b32 m0, s37
	s_nop 0
	global_load_lds_dwordx4 v[212:213], off
	s_mov_b32 m0, s31
	s_nop 0
	global_load_lds_dwordx4 v215, s[20:21]
	s_mov_b32 m0, s40
	s_nop 0
	global_load_lds_dwordx4 v216, s[20:21]
	s_waitcnt vmcnt(8)
	s_waitcnt lgkmcnt(0)
	s_barrier
	s_setprio 1
	s_waitcnt lgkmcnt(0)
	v_mfma_scale_f32_16x16x128_f8f6f4 v[94:97], v[18:25], v[222:229], 0, v172, v172 op_sel_hi:[0,0,0]
	v_mfma_scale_f32_16x16x128_f8f6f4 v[86:89], v[26:33], v[222:229], 0, v172, v172 op_sel_hi:[0,0,0]
	v_mfma_scale_f32_16x16x128_f8f6f4 v[78:81], v[18:25], v[230:237], 0, v172, v172 op_sel_hi:[0,0,0]
	v_mfma_scale_f32_16x16x128_f8f6f4 v[70:73], v[26:33], v[230:237], 0, v172, v172 op_sel_hi:[0,0,0]
	v_mfma_scale_f32_16x16x128_f8f6f4 v[62:65], v[18:25], v[238:245], 0, v172, v172 op_sel_hi:[0,0,0]
	v_mfma_scale_f32_16x16x128_f8f6f4 v[54:57], v[26:33], v[238:245], 0, v172, v172 op_sel_hi:[0,0,0]
	v_mfma_scale_f32_16x16x128_f8f6f4 v[46:49], v[18:25], v[246:253], 0, v172, v172 op_sel_hi:[0,0,0]
	v_mfma_scale_f32_16x16x128_f8f6f4 v[38:41], v[26:33], v[246:253], 0, v172, v172 op_sel_hi:[0,0,0]
	s_setprio 0
	s_setprio 1
	v_mfma_scale_f32_16x16x128_f8f6f4 v[90:93], v[2:9], v[222:229], 0, v172, v172 op_sel_hi:[0,0,0]
	v_mfma_scale_f32_16x16x128_f8f6f4 v[82:85], v[10:17], v[222:229], 0, v172, v172 op_sel_hi:[0,0,0]
	v_mfma_scale_f32_16x16x128_f8f6f4 v[74:77], v[2:9], v[230:237], 0, v172, v172 op_sel_hi:[0,0,0]
	v_mfma_scale_f32_16x16x128_f8f6f4 v[66:69], v[10:17], v[230:237], 0, v172, v172 op_sel_hi:[0,0,0]
	v_mfma_scale_f32_16x16x128_f8f6f4 v[58:61], v[2:9], v[238:245], 0, v172, v172 op_sel_hi:[0,0,0]
	v_mfma_scale_f32_16x16x128_f8f6f4 v[50:53], v[10:17], v[238:245], 0, v172, v172 op_sel_hi:[0,0,0]
	v_mfma_scale_f32_16x16x128_f8f6f4 v[42:45], v[2:9], v[246:253], 0, v172, v172 op_sel_hi:[0,0,0]
	v_mfma_scale_f32_16x16x128_f8f6f4 v[34:37], v[10:17], v[246:253], 0, v172, v172 op_sel_hi:[0,0,0]
	s_setprio 0
	s_barrier
	ds_read_b32 v2, v0 offset:512
	s_waitcnt lgkmcnt(0)
	v_lshl_or_b32 v212, v2, 10, v173
	ds_read_b32 v2, v214 offset:512
	s_waitcnt lgkmcnt(0)
	v_lshl_or_b32 v213, v2, 10, v173
	ds_read_b128 v[2:5], v179
	ds_read_b128 v[6:9], v195
	ds_read_b128 v[18:21], v180
	ds_read_b128 v[22:25], v196
	ds_read_b128 v[10:13], v181
	ds_read_b128 v[14:17], v197
	ds_read_b128 v[26:29], v182
	ds_read_b128 v[30:33], v198
	s_mov_b32 m0, s41
	ds_read_b128 v[222:225], v211 offset:32768
	ds_read_b128 v[230:233], v211 offset:34816
	ds_read_b128 v[226:229], v199
	ds_read_b128 v[234:237], v200
	ds_read_b128 v[238:241], v211 offset:36864
	ds_read_b128 v[246:249], v211 offset:38912
	ds_read_b128 v[242:245], v201
	ds_read_b128 v[250:253], v202
	global_load_lds_dwordx4 v212, s[20:21]
	s_mov_b32 m0, s42
	s_nop 0
	global_load_lds_dwordx4 v213, s[20:21]
	s_waitcnt vmcnt(8)
	s_waitcnt lgkmcnt(0)
	s_barrier
	s_setprio 1
	s_waitcnt lgkmcnt(0)
	v_mfma_scale_f32_16x16x128_f8f6f4 v[158:161], v[2:9], v[222:229], v[158:161], v172, v172 op_sel_hi:[0,0,0]
	v_mfma_scale_f32_16x16x128_f8f6f4 v[150:153], v[18:25], v[222:229], v[150:153], v172, v172 op_sel_hi:[0,0,0]
	v_mfma_scale_f32_16x16x128_f8f6f4 v[142:145], v[2:9], v[230:237], v[142:145], v172, v172 op_sel_hi:[0,0,0]
	v_mfma_scale_f32_16x16x128_f8f6f4 v[134:137], v[18:25], v[230:237], v[134:137], v172, v172 op_sel_hi:[0,0,0]
	v_mfma_scale_f32_16x16x128_f8f6f4 v[126:129], v[2:9], v[238:245], v[126:129], v172, v172 op_sel_hi:[0,0,0]
	v_mfma_scale_f32_16x16x128_f8f6f4 v[118:121], v[18:25], v[238:245], v[118:121], v172, v172 op_sel_hi:[0,0,0]
	v_mfma_scale_f32_16x16x128_f8f6f4 v[110:113], v[2:9], v[246:253], v[110:113], v172, v172 op_sel_hi:[0,0,0]
	v_mfma_scale_f32_16x16x128_f8f6f4 v[102:105], v[18:25], v[246:253], v[102:105], v172, v172 op_sel_hi:[0,0,0]
	s_setprio 0
	s_setprio 1
	v_mfma_scale_f32_16x16x128_f8f6f4 v[154:157], v[10:17], v[222:229], v[154:157], v172, v172 op_sel_hi:[0,0,0]
	v_mfma_scale_f32_16x16x128_f8f6f4 v[146:149], v[26:33], v[222:229], v[146:149], v172, v172 op_sel_hi:[0,0,0]
	v_mfma_scale_f32_16x16x128_f8f6f4 v[138:141], v[10:17], v[230:237], v[138:141], v172, v172 op_sel_hi:[0,0,0]
	v_mfma_scale_f32_16x16x128_f8f6f4 v[130:133], v[26:33], v[230:237], v[130:133], v172, v172 op_sel_hi:[0,0,0]
	v_mfma_scale_f32_16x16x128_f8f6f4 v[122:125], v[10:17], v[238:245], v[122:125], v172, v172 op_sel_hi:[0,0,0]
	v_mfma_scale_f32_16x16x128_f8f6f4 v[114:117], v[26:33], v[238:245], v[114:117], v172, v172 op_sel_hi:[0,0,0]
	v_mfma_scale_f32_16x16x128_f8f6f4 v[106:109], v[10:17], v[246:253], v[106:109], v172, v172 op_sel_hi:[0,0,0]
	v_mfma_scale_f32_16x16x128_f8f6f4 v[98:101], v[26:33], v[246:253], v[98:101], v172, v172 op_sel_hi:[0,0,0]
	s_setprio 0
	s_barrier
	s_mov_b32 m0, s43
	ds_read_b32 v0, v0
	ds_read_b32 v212, v214
	ds_read_b128 v[226:229], v203
	v_lshl_add_u64 v[166:167], v[166:167], 0, s[78:79]
	s_add_u32 s22, s22, 0x20080
	ds_read_b128 v[222:225], v211 offset:49152
	ds_read_b128 v[230:233], v211 offset:51200
	ds_read_b128 v[234:237], v206
	ds_read_b128 v[242:245], v207
	ds_read_b128 v[238:241], v211 offset:53248
	ds_read_b128 v[246:249], v211 offset:55296
	ds_read_b128 v[250:253], v208
	global_load_lds_dwordx4 v[166:167], off
	v_lshl_add_u64 v[166:167], v[168:169], 0, s[78:79]
	s_mov_b32 m0, s44
	s_addc_u32 s23, s23, 0
	global_load_lds_dwordx4 v[166:167], off
	v_lshl_add_u64 v[166:167], s[22:23], 0, v[164:165]
	s_mov_b32 m0, s51
	s_waitcnt lgkmcnt(0)
	v_lshl_or_b32 v0, v0, 10, v173
	global_load_lds_dwordx4 v[166:167], off
	v_lshl_add_u64 v[166:167], s[22:23], 0, v[162:163]
	s_mov_b32 m0, s52
	v_lshl_or_b32 v212, v212, 10, v173
	global_load_lds_dwordx4 v[166:167], off
	v_lshl_add_u64 v[166:167], s[20:21], 0, v[0:1]
	v_lshl_add_u64 v[166:167], v[166:167], 0, s[78:79]
	s_mov_b32 m0, s45
	v_mov_b32_e32 v213, v1
	global_load_lds_dwordx4 v[166:167], off
	v_lshl_add_u64 v[166:167], s[20:21], 0, v[212:213]
	v_lshl_add_u64 v[166:167], v[166:167], 0, s[78:79]
	s_mov_b32 m0, s48
	s_nop 0
	global_load_lds_dwordx4 v[166:167], off
	s_waitcnt vmcnt(8)
	s_waitcnt lgkmcnt(0)
	s_barrier
	s_setprio 1
	v_mfma_scale_f32_16x16x128_f8f6f4 v[94:97], v[2:9], v[222:229], v[94:97], v172, v172 op_sel_hi:[0,0,0]
	v_mfma_scale_f32_16x16x128_f8f6f4 v[86:89], v[18:25], v[222:229], v[86:89], v172, v172 op_sel_hi:[0,0,0]
	v_mfma_scale_f32_16x16x128_f8f6f4 v[78:81], v[2:9], v[230:237], v[78:81], v172, v172 op_sel_hi:[0,0,0]
	v_mfma_scale_f32_16x16x128_f8f6f4 v[70:73], v[18:25], v[230:237], v[70:73], v172, v172 op_sel_hi:[0,0,0]
	v_mfma_scale_f32_16x16x128_f8f6f4 v[62:65], v[2:9], v[238:245], v[62:65], v172, v172 op_sel_hi:[0,0,0]
	v_mfma_scale_f32_16x16x128_f8f6f4 v[54:57], v[18:25], v[238:245], v[54:57], v172, v172 op_sel_hi:[0,0,0]
	v_mfma_scale_f32_16x16x128_f8f6f4 v[46:49], v[2:9], v[246:253], v[46:49], v172, v172 op_sel_hi:[0,0,0]
	v_mfma_scale_f32_16x16x128_f8f6f4 v[38:41], v[18:25], v[246:253], v[38:41], v172, v172 op_sel_hi:[0,0,0]
	s_setprio 0
	s_setprio 1
	v_mfma_scale_f32_16x16x128_f8f6f4 v[90:93], v[10:17], v[222:229], v[90:93], v172, v172 op_sel_hi:[0,0,0]
	v_mfma_scale_f32_16x16x128_f8f6f4 v[82:85], v[26:33], v[222:229], v[82:85], v172, v172 op_sel_hi:[0,0,0]
	v_mfma_scale_f32_16x16x128_f8f6f4 v[74:77], v[10:17], v[230:237], v[74:77], v172, v172 op_sel_hi:[0,0,0]
	v_mfma_scale_f32_16x16x128_f8f6f4 v[66:69], v[26:33], v[230:237], v[66:69], v172, v172 op_sel_hi:[0,0,0]
	v_mfma_scale_f32_16x16x128_f8f6f4 v[58:61], v[10:17], v[238:245], v[58:61], v172, v172 op_sel_hi:[0,0,0]
	v_mfma_scale_f32_16x16x128_f8f6f4 v[50:53], v[26:33], v[238:245], v[50:53], v172, v172 op_sel_hi:[0,0,0]
	v_mfma_scale_f32_16x16x128_f8f6f4 v[42:45], v[10:17], v[246:253], v[42:45], v172, v172 op_sel_hi:[0,0,0]
	v_mfma_scale_f32_16x16x128_f8f6f4 v[34:37], v[26:33], v[246:253], v[34:37], v172, v172 op_sel_hi:[0,0,0]
	s_setprio 0
	s_barrier
	s_add_i32 s70, s70, 2
	s_add_u32 s18, s18, 0x100
	s_addc_u32 s19, s19, 0
	s_add_u32 s68, s68, 0x100
	s_addc_u32 s69, s69, 0
	s_cmp_gt_u32 s70, 5

.LBB0_1871:
	s_nop 0
	s_nop 0
	s_nop 0
	s_nop 0
	s_nop 0
	s_nop 0
	s_nop 0
	s_nop 0
	s_nop 0
	s_add_u32 s13, s20, 0x100
	s_addc_u32 s49, s21, 0
	s_mov_b32 s68, -2
	ds_read_b128 v[18:21], v182
	ds_read_b128 v[26:29], v183
	ds_read_b128 v[22:25], v193
	ds_read_b128 v[30:33], v194
	ds_read_b128 v[2:5], v184
	ds_read_b128 v[10:13], v185
	ds_read_b128 v[6:9], v195
	ds_read_b128 v[14:17], v196
	s_add_u32 s20, s18, 0x100
	s_addc_u32 s21, s19, 0
	s_cmp_eq_u32 s68, 4
	s_cselect_b32 s25, s15, s21
	s_cselect_b32 s24, s14, s20
	s_cselect_b32 s23, s17, s49
	s_cselect_b32 s22, s16, s13
	v_add_u32_e32 v234, 0, v181
	v_lshl_add_u64 v[212:213], s[18:19], 0, v[168:169]
	s_add_i32 m0, s36, 0xc000
	ds_read_b128 v[172:175], v234
	ds_read_b128 v[222:225], v234 offset:2048
	ds_read_b128 v[176:179], v197
	ds_read_b128 v[226:229], v197 offset:2048
	ds_read_b128 v[236:239], v234 offset:4096
	ds_read_b128 v[244:247], v234 offset:6144
	ds_read_b128 v[240:243], v197 offset:4096
	ds_read_b128 v[248:251], v197 offset:6144
	global_load_lds_dwordx4 v[212:213], off
	v_lshl_add_u64 v[212:213], s[18:19], 0, v[170:171]
	s_add_i32 m0, s36, 0xe000
	s_nop 0
	global_load_lds_dwordx4 v[212:213], off
	s_waitcnt vmcnt(8)
	s_waitcnt lgkmcnt(0)
	s_barrier
	s_setprio 1
	s_waitcnt lgkmcnt(0)
	v_mfma_scale_f32_16x16x128_f8f6f4 v[158:161], v[18:25], v[172:179], 0, v180, v180 op_sel_hi:[0,0,0]
	v_mfma_scale_f32_16x16x128_f8f6f4 v[154:157], v[26:33], v[172:179], 0, v180, v180 op_sel_hi:[0,0,0]
	v_mfma_scale_f32_16x16x128_f8f6f4 v[150:153], v[18:25], v[222:229], 0, v180, v180 op_sel_hi:[0,0,0]
	v_mfma_scale_f32_16x16x128_f8f6f4 v[146:149], v[26:33], v[222:229], 0, v180, v180 op_sel_hi:[0,0,0]
	v_mfma_scale_f32_16x16x128_f8f6f4 v[126:129], v[18:25], v[236:243], 0, v180, v180 op_sel_hi:[0,0,0]
	v_mfma_scale_f32_16x16x128_f8f6f4 v[122:125], v[26:33], v[236:243], 0, v180, v180 op_sel_hi:[0,0,0]
	v_mfma_scale_f32_16x16x128_f8f6f4 v[118:121], v[18:25], v[244:251], 0, v180, v180 op_sel_hi:[0,0,0]
	v_mfma_scale_f32_16x16x128_f8f6f4 v[114:117], v[26:33], v[244:251], 0, v180, v180 op_sel_hi:[0,0,0]
	s_setprio 0
	s_setprio 1
	v_mfma_scale_f32_16x16x128_f8f6f4 v[142:145], v[2:9], v[172:179], 0, v180, v180 op_sel_hi:[0,0,0]
	v_mfma_scale_f32_16x16x128_f8f6f4 v[138:141], v[10:17], v[172:179], 0, v180, v180 op_sel_hi:[0,0,0]
	v_mfma_scale_f32_16x16x128_f8f6f4 v[134:137], v[2:9], v[222:229], 0, v180, v180 op_sel_hi:[0,0,0]
	v_mfma_scale_f32_16x16x128_f8f6f4 v[130:133], v[10:17], v[222:229], 0, v180, v180 op_sel_hi:[0,0,0]
	v_mfma_scale_f32_16x16x128_f8f6f4 v[110:113], v[2:9], v[236:243], 0, v180, v180 op_sel_hi:[0,0,0]
	v_mfma_scale_f32_16x16x128_f8f6f4 v[106:109], v[10:17], v[236:243], 0, v180, v180 op_sel_hi:[0,0,0]
	v_mfma_scale_f32_16x16x128_f8f6f4 v[102:105], v[2:9], v[244:251], 0, v180, v180 op_sel_hi:[0,0,0]
	v_mfma_scale_f32_16x16x128_f8f6f4 v[98:101], v[10:17], v[244:251], 0, v180, v180 op_sel_hi:[0,0,0]
	s_setprio 0
	s_barrier
	s_mov_b32 m0, s37
	v_lshl_add_u64 v[172:173], s[22:23], 0, v[0:1]
	s_add_u32 s18, s22, 0x20000
	ds_read_b128 v[222:225], v234 offset:16384
	ds_read_b128 v[236:239], v234 offset:18432
	ds_read_b128 v[226:229], v198
	ds_read_b128 v[240:243], v199
	ds_read_b128 v[244:247], v234 offset:20480
	ds_read_b128 v[212:215], v234 offset:22528
	ds_read_b128 v[248:251], v200
	ds_read_b128 v[216:219], v201
	global_load_lds_dwordx4 v[172:173], off
	v_lshl_add_u64 v[174:175], s[22:23], 0, v[162:163]
	s_mov_b32 m0, s40
	s_addc_u32 s19, s23, 0
	global_load_lds_dwordx4 v[174:175], off
	v_lshl_add_u64 v[176:177], s[18:19], 0, v[0:1]
	s_mov_b32 m0, s41
	v_lshl_add_u64 v[178:179], s[24:25], 0, v[166:167]
	global_load_lds_dwordx4 v[176:177], off
	v_lshl_add_u64 v[176:177], s[18:19], 0, v[162:163]
	s_mov_b32 m0, s42
	s_nop 0
	global_load_lds_dwordx4 v[176:177], off
	v_lshl_add_u64 v[176:177], s[24:25], 0, v[164:165]
	s_mov_b32 m0, s36
	s_nop 0
	global_load_lds_dwordx4 v[176:177], off
	s_mov_b32 m0, s43
	s_nop 0
	global_load_lds_dwordx4 v[178:179], off
	s_waitcnt vmcnt(8)
	s_waitcnt lgkmcnt(0)
	s_barrier
	s_setprio 1
	s_waitcnt lgkmcnt(0)
	v_mfma_scale_f32_16x16x128_f8f6f4 v[94:97], v[18:25], v[222:229], 0, v180, v180 op_sel_hi:[0,0,0]
	v_mfma_scale_f32_16x16x128_f8f6f4 v[90:93], v[26:33], v[222:229], 0, v180, v180 op_sel_hi:[0,0,0]
	v_mfma_scale_f32_16x16x128_f8f6f4 v[86:89], v[18:25], v[236:243], 0, v180, v180 op_sel_hi:[0,0,0]
	v_mfma_scale_f32_16x16x128_f8f6f4 v[82:85], v[26:33], v[236:243], 0, v180, v180 op_sel_hi:[0,0,0]
	v_mfma_scale_f32_16x16x128_f8f6f4 v[62:65], v[18:25], v[244:251], 0, v180, v180 op_sel_hi:[0,0,0]
	v_mfma_scale_f32_16x16x128_f8f6f4 v[58:61], v[26:33], v[244:251], 0, v180, v180 op_sel_hi:[0,0,0]
	v_mfma_scale_f32_16x16x128_f8f6f4 v[54:57], v[18:25], v[212:219], 0, v180, v180 op_sel_hi:[0,0,0]
	v_mfma_scale_f32_16x16x128_f8f6f4 v[50:53], v[26:33], v[212:219], 0, v180, v180 op_sel_hi:[0,0,0]
	s_setprio 0
	s_setprio 1
	v_mfma_scale_f32_16x16x128_f8f6f4 v[78:81], v[2:9], v[222:229], 0, v180, v180 op_sel_hi:[0,0,0]
	v_mfma_scale_f32_16x16x128_f8f6f4 v[74:77], v[10:17], v[222:229], 0, v180, v180 op_sel_hi:[0,0,0]
	v_mfma_scale_f32_16x16x128_f8f6f4 v[70:73], v[2:9], v[236:243], 0, v180, v180 op_sel_hi:[0,0,0]
	v_mfma_scale_f32_16x16x128_f8f6f4 v[66:69], v[10:17], v[236:243], 0, v180, v180 op_sel_hi:[0,0,0]
	v_mfma_scale_f32_16x16x128_f8f6f4 v[46:49], v[2:9], v[244:251], 0, v180, v180 op_sel_hi:[0,0,0]
	v_mfma_scale_f32_16x16x128_f8f6f4 v[42:45], v[10:17], v[244:251], 0, v180, v180 op_sel_hi:[0,0,0]
	v_mfma_scale_f32_16x16x128_f8f6f4 v[38:41], v[2:9], v[212:219], 0, v180, v180 op_sel_hi:[0,0,0]
	v_mfma_scale_f32_16x16x128_f8f6f4 v[34:37], v[10:17], v[212:219], 0, v180, v180 op_sel_hi:[0,0,0]
	s_setprio 0
	s_barrier
	ds_read_b128 v[2:5], v186
	ds_read_b128 v[10:13], v187
	ds_read_b128 v[6:9], v202
	ds_read_b128 v[14:17], v203
	ds_read_b128 v[18:21], v188
	ds_read_b128 v[26:29], v189
	ds_read_b128 v[22:25], v206
	ds_read_b128 v[30:33], v207
	s_add_u32 s18, s24, 0x20000
	s_addc_u32 s19, s25, 0
	s_mov_b32 m0, s44
	v_lshl_add_u64 v[252:253], s[18:19], 0, v[164:165]
	ds_read_b128 v[212:215], v234 offset:32768
	ds_read_b128 v[222:225], v234 offset:34816
	ds_read_b128 v[216:219], v208
	ds_read_b128 v[226:229], v209
	ds_read_b128 v[236:239], v234 offset:36864
	ds_read_b128 v[244:247], v234 offset:38912
	ds_read_b128 v[240:243], v210
	ds_read_b128 v[248:251], v211
	global_load_lds_dwordx4 v[252:253], off
	v_lshl_add_u64 v[252:253], s[18:19], 0, v[166:167]
	s_mov_b32 m0, s45
	s_nop 0
	global_load_lds_dwordx4 v[252:253], off
	s_waitcnt vmcnt(8)
	s_waitcnt lgkmcnt(0)
	s_barrier
	s_setprio 1
	s_waitcnt lgkmcnt(0)
	v_mfma_scale_f32_16x16x128_f8f6f4 v[158:161], v[2:9], v[212:219], v[158:161], v180, v180 op_sel_hi:[0,0,0]
	v_mfma_scale_f32_16x16x128_f8f6f4 v[154:157], v[10:17], v[212:219], v[154:157], v180, v180 op_sel_hi:[0,0,0]
	v_mfma_scale_f32_16x16x128_f8f6f4 v[150:153], v[2:9], v[222:229], v[150:153], v180, v180 op_sel_hi:[0,0,0]
	v_mfma_scale_f32_16x16x128_f8f6f4 v[146:149], v[10:17], v[222:229], v[146:149], v180, v180 op_sel_hi:[0,0,0]
	v_mfma_scale_f32_16x16x128_f8f6f4 v[126:129], v[2:9], v[236:243], v[126:129], v180, v180 op_sel_hi:[0,0,0]
	v_mfma_scale_f32_16x16x128_f8f6f4 v[122:125], v[10:17], v[236:243], v[122:125], v180, v180 op_sel_hi:[0,0,0]
	v_mfma_scale_f32_16x16x128_f8f6f4 v[118:121], v[2:9], v[244:251], v[118:121], v180, v180 op_sel_hi:[0,0,0]
	v_mfma_scale_f32_16x16x128_f8f6f4 v[114:117], v[10:17], v[244:251], v[114:117], v180, v180 op_sel_hi:[0,0,0]
	s_setprio 0
	s_setprio 1
	v_mfma_scale_f32_16x16x128_f8f6f4 v[142:145], v[18:25], v[212:219], v[142:145], v180, v180 op_sel_hi:[0,0,0]
	v_mfma_scale_f32_16x16x128_f8f6f4 v[138:141], v[26:33], v[212:219], v[138:141], v180, v180 op_sel_hi:[0,0,0]
	v_mfma_scale_f32_16x16x128_f8f6f4 v[134:137], v[18:25], v[222:229], v[134:137], v180, v180 op_sel_hi:[0,0,0]
	v_mfma_scale_f32_16x16x128_f8f6f4 v[130:133], v[26:33], v[222:229], v[130:133], v180, v180 op_sel_hi:[0,0,0]
	v_mfma_scale_f32_16x16x128_f8f6f4 v[110:113], v[18:25], v[236:243], v[110:113], v180, v180 op_sel_hi:[0,0,0]
	v_mfma_scale_f32_16x16x128_f8f6f4 v[106:109], v[26:33], v[236:243], v[106:109], v180, v180 op_sel_hi:[0,0,0]
	v_mfma_scale_f32_16x16x128_f8f6f4 v[102:105], v[18:25], v[244:251], v[102:105], v180, v180 op_sel_hi:[0,0,0]
	v_mfma_scale_f32_16x16x128_f8f6f4 v[98:101], v[26:33], v[244:251], v[98:101], v180, v180 op_sel_hi:[0,0,0]
	s_setprio 0
	s_barrier
	s_mov_b32 m0, s46
	v_lshl_add_u64 v[172:173], v[172:173], 0, s[78:79]
	s_add_u32 s18, s22, 0x20080
	ds_read_b128 v[212:215], v234 offset:49152
	ds_read_b128 v[222:225], v234 offset:51200
	ds_read_b128 v[216:219], v230
	ds_read_b128 v[226:229], v231
	ds_read_b128 v[236:239], v234 offset:53248
	ds_read_b128 v[244:247], v234 offset:55296
	ds_read_b128 v[240:243], v232
	ds_read_b128 v[248:251], v233
	global_load_lds_dwordx4 v[172:173], off
	v_lshl_add_u64 v[172:173], v[174:175], 0, s[78:79]
	s_mov_b32 m0, s48
	s_addc_u32 s19, s23, 0
	global_load_lds_dwordx4 v[172:173], off
	v_lshl_add_u64 v[172:173], s[18:19], 0, v[0:1]
	s_mov_b32 m0, s53
	s_nop 0
	global_load_lds_dwordx4 v[172:173], off
	v_lshl_add_u64 v[172:173], s[18:19], 0, v[162:163]
	s_mov_b32 m0, s54
	s_nop 0
	global_load_lds_dwordx4 v[172:173], off
	v_lshl_add_u64 v[172:173], v[176:177], 0, s[78:79]
	s_mov_b32 m0, s51
	s_nop 0
	global_load_lds_dwordx4 v[172:173], off
	v_lshl_add_u64 v[172:173], v[178:179], 0, s[78:79]
	s_mov_b32 m0, s52
	s_nop 0
	global_load_lds_dwordx4 v[172:173], off
	s_waitcnt vmcnt(8)
	s_waitcnt lgkmcnt(0)
	s_barrier
	s_setprio 1
	s_waitcnt lgkmcnt(0)
	v_mfma_scale_f32_16x16x128_f8f6f4 v[94:97], v[2:9], v[212:219], v[94:97], v180, v180 op_sel_hi:[0,0,0]
	v_mfma_scale_f32_16x16x128_f8f6f4 v[90:93], v[10:17], v[212:219], v[90:93], v180, v180 op_sel_hi:[0,0,0]
	v_mfma_scale_f32_16x16x128_f8f6f4 v[86:89], v[2:9], v[222:229], v[86:89], v180, v180 op_sel_hi:[0,0,0]
	v_mfma_scale_f32_16x16x128_f8f6f4 v[82:85], v[10:17], v[222:229], v[82:85], v180, v180 op_sel_hi:[0,0,0]
	v_mfma_scale_f32_16x16x128_f8f6f4 v[62:65], v[2:9], v[236:243], v[62:65], v180, v180 op_sel_hi:[0,0,0]
	v_mfma_scale_f32_16x16x128_f8f6f4 v[58:61], v[10:17], v[236:243], v[58:61], v180, v180 op_sel_hi:[0,0,0]
	v_mfma_scale_f32_16x16x128_f8f6f4 v[54:57], v[2:9], v[244:251], v[54:57], v180, v180 op_sel_hi:[0,0,0]
	v_mfma_scale_f32_16x16x128_f8f6f4 v[50:53], v[10:17], v[244:251], v[50:53], v180, v180 op_sel_hi:[0,0,0]
	s_setprio 0
	s_setprio 1
	v_mfma_scale_f32_16x16x128_f8f6f4 v[78:81], v[18:25], v[212:219], v[78:81], v180, v180 op_sel_hi:[0,0,0]
	v_mfma_scale_f32_16x16x128_f8f6f4 v[74:77], v[26:33], v[212:219], v[74:77], v180, v180 op_sel_hi:[0,0,0]
	v_mfma_scale_f32_16x16x128_f8f6f4 v[70:73], v[18:25], v[222:229], v[70:73], v180, v180 op_sel_hi:[0,0,0]
	v_mfma_scale_f32_16x16x128_f8f6f4 v[66:69], v[26:33], v[222:229], v[66:69], v180, v180 op_sel_hi:[0,0,0]
	v_mfma_scale_f32_16x16x128_f8f6f4 v[46:49], v[18:25], v[236:243], v[46:49], v180, v180 op_sel_hi:[0,0,0]
	v_mfma_scale_f32_16x16x128_f8f6f4 v[42:45], v[26:33], v[236:243], v[42:45], v180, v180 op_sel_hi:[0,0,0]
	v_mfma_scale_f32_16x16x128_f8f6f4 v[38:41], v[18:25], v[244:251], v[38:41], v180, v180 op_sel_hi:[0,0,0]
	v_mfma_scale_f32_16x16x128_f8f6f4 v[34:37], v[26:33], v[244:251], v[34:37], v180, v180 op_sel_hi:[0,0,0]
	s_setprio 0
	s_barrier
	s_add_i32 s68, s68, 2
	s_add_u32 s13, s13, 0x100
	s_addc_u32 s49, s49, 0
	s_cmp_gt_u32 s68, 5
	s_mov_b64 s[18:19], s[20:21]
